# v90 + attention gate over row-sum quotients by v_rcp_f32 times numerator instead of the expanded IEEE division (4 sites)
# speedup vs baseline: 1.0013x; 1.0013x over previous
; __device__ __forceinline__ unsigned cvt_pk_bf16(float lo, float hi) { const f32x2_t v = {lo, hi}; const bf16x2_t b = __builtin_convertvector(v, bf16x2_t); return __builtin_bit_cast(unsigned, b); }
; #define GATE(rb, br) (GATES[TOKROW(rb) * 48 + head * 3 + (br)])
; __device__ __forceinline__ void ph_attn_fast2(const Args& a, LAS unsigned char* lds) {
;     ...
;                 for (int rb = 0; rb < 2; ++rb) { const float l = __shfl(ss[rb].ol[0], fr); const float sc1 = (l > 0.f) ? GATE(rb, 1) / l : 0.f;
;                     bf16_t* op = O + TOKROW(rb) * 1024 + head * 64 + 4 * g4;
; #pragma unroll
;                     for (int dt = 0; dt < 4; ++dt) { const u32x2 pv = *(const u32x2*)(op + 16 * dt); f32x4 v = ss[rb].o[dt] * sc1;
;                         v[0] += __uint_as_float(pv.x << 16); v[1] += __uint_as_float(pv.x & 0xffff0000u); v[2] += __uint_as_float(pv.y << 16); v[3] += __uint_as_float(pv.y & 0xffff0000u);
;                         u32x2 w; w.x = cvt_pk_bf16(v[0], v[1]); w.y = cvt_pk_bf16(v[2], v[3]); *(u32x2*)(op + 16 * dt) = w; } }
.LBB0_2117:
	ds_bpermute_b32 v1, v243, v62
	s_xor_b64 s[0:1], s[6:7], -1
	v_mov_b32_e32 v2, 0
	v_ashrrev_i32_e32 v109, 31, v108
	s_waitcnt lgkmcnt(0)
	v_cmp_lt_f32_e32 vcc, 0, v1
	v_mov_b32_e32 v4, 0
	s_and_saveexec_b64 s[2:3], vcc
	v_readlane_b32 s25, v251, 8
	v_readlane_b32 s8, v252, 61
	v_readlane_b32 s9, v252, 62
	s_cbranch_execz .LBB0_2119
	v_readlane_b32 s6, v252, 59
	v_readlane_b32 s7, v252, 60
	s_movk_i32 s5, 0xc0
	s_nop 0
	v_lshl_add_u64 v[4:5], s[6:7], 0, v[108:109]
	v_mad_u64_u32 v[36:37], s[6:7], v4, s5, v[174:175]
	v_mad_i32_i24 v37, v5, s5, v37
	global_load_dword v4, v[36:37], off offset:4
	s_waitcnt vmcnt(0)
	v_rcp_f32_e32 v5, v1
	s_nop 0
	v_mul_f32_e32 v4, v4, v5
.LBB0_2119:
	s_or_b64 exec, exec, s[2:3]
	v_lshlrev_b64 v[36:37], 11, v[108:109]
	v_lshl_add_u64 v[36:37], v[178:179], 0, v[36:37]
	global_load_dwordx2 v[62:63], v[36:37], off
	global_load_dwordx2 v[66:67], v[36:37], off offset:32
	global_load_dwordx2 v[68:69], v[36:37], off offset:64
	global_load_dwordx2 v[70:71], v[36:37], off offset:96
	ds_bpermute_b32 v1, v243, v34
	v_ashrrev_i32_e32 v107, 31, v106
	s_waitcnt lgkmcnt(0)
	v_cmp_lt_f32_e32 vcc, 0, v1
	s_waitcnt vmcnt(0)
	v_lshlrev_b32_e32 v64, 16, v62
	v_and_b32_e32 v65, 0xffff0000, v62
	v_lshlrev_b32_e32 v62, 16, v63
	v_and_b32_e32 v63, 0xffff0000, v63
	v_pk_fma_f32 v[46:47], v[46:47], v[4:5], v[64:65] op_sel_hi:[1,0,1]
	v_pk_fma_f32 v[48:49], v[48:49], v[4:5], v[62:63] op_sel_hi:[1,0,1]
	v_cvt_pk_bf16_f32 v46, v46, v47
	v_cvt_pk_bf16_f32 v47, v48, v49
	global_store_dwordx2 v[36:37], v[46:47], off
	v_lshlrev_b32_e32 v48, 16, v66
	v_and_b32_e32 v49, 0xffff0000, v66
	v_lshlrev_b32_e32 v46, 16, v67
	v_and_b32_e32 v47, 0xffff0000, v67
	v_pk_fma_f32 v[48:49], v[50:51], v[4:5], v[48:49] op_sel_hi:[1,0,1]
	v_pk_fma_f32 v[46:47], v[52:53], v[4:5], v[46:47] op_sel_hi:[1,0,1]
	v_cvt_pk_bf16_f32 v48, v48, v49
	v_cvt_pk_bf16_f32 v49, v46, v47
	global_store_dwordx2 v[36:37], v[48:49], off offset:32
	v_lshlrev_b32_e32 v48, 16, v68
	v_and_b32_e32 v49, 0xffff0000, v68
	v_lshlrev_b32_e32 v46, 16, v69
	v_and_b32_e32 v47, 0xffff0000, v69
	v_pk_fma_f32 v[48:49], v[54:55], v[4:5], v[48:49] op_sel_hi:[1,0,1]
	v_pk_fma_f32 v[46:47], v[56:57], v[4:5], v[46:47] op_sel_hi:[1,0,1]
	v_cvt_pk_bf16_f32 v48, v48, v49
	v_cvt_pk_bf16_f32 v49, v46, v47
	global_store_dwordx2 v[36:37], v[48:49], off offset:64
	v_lshlrev_b32_e32 v48, 16, v70
	v_and_b32_e32 v49, 0xffff0000, v70
	v_lshlrev_b32_e32 v46, 16, v71
	v_and_b32_e32 v47, 0xffff0000, v71
	v_pk_fma_f32 v[48:49], v[58:59], v[4:5], v[48:49] op_sel_hi:[1,0,1]
	v_pk_fma_f32 v[4:5], v[60:61], v[4:5], v[46:47] op_sel_hi:[1,0,1]
	v_cvt_pk_bf16_f32 v46, v48, v49
	v_cvt_pk_bf16_f32 v47, v4, v5
	global_store_dwordx2 v[36:37], v[46:47], off offset:96
	s_and_saveexec_b64 s[2:3], vcc
	s_cbranch_execz .LBB0_2121
	v_readlane_b32 s6, v252, 59
	v_readlane_b32 s7, v252, 60
	s_movk_i32 s5, 0xc0
	s_nop 0
	v_lshl_add_u64 v[4:5], s[6:7], 0, v[106:107]
	v_mad_u64_u32 v[34:35], s[6:7], v4, s5, v[174:175]
	v_mad_i32_i24 v35, v5, s5, v35
	global_load_dword v2, v[34:35], off offset:4
	s_waitcnt vmcnt(0)
	v_rcp_f32_e32 v4, v1
	s_nop 0
	v_mul_f32_e32 v2, v2, v4

; __device__ __forceinline__ unsigned pk4_fp8(float a, float b, float c, float d) { int w = __builtin_amdgcn_cvt_pk_fp8_f32(a, b, 0, false); return (unsigned)__builtin_amdgcn_cvt_pk_fp8_f32(c, d, w, true); }
; __device__ __forceinline__ float clamp8(float v) { return __builtin_amdgcn_fmed3f(v, -448.0f, 448.0f); }
; #define GATE(rb, br) (GATES[TOKROW(rb) * 48 + head * 3 + (br)])
; __device__ __forceinline__ void ph_attn_fast2(const Args& a, LAS unsigned char* lds) {
;     ...
;                 for (int rb = 0; rb < 2; ++rb) { const float l = __shfl(ss[rb].ol[0], fr); const float sc1 = (l > 0.f) ? GATE(rb, 1) / l : 0.f;
;     ...
;                 for (int rb = 0; rb < 2; ++rb) { const float l = __shfl(sw[rb].ol[0], fr); const float sc2 = (l > 0.f) ? GATE(rb, 2) / l : 0.f;
;                     bf16_t* op = O + TOKROW(rb) * 1024 + head * 64 + 4 * g4;
;                     unsigned char* o8 = (unsigned char*)(a.ws + WS_O8) + TOKROW(rb) * 1024 + head * 64 + 4 * g4;
; #pragma unroll
;                     for (int dt = 0; dt < 4; ++dt) { const u32x2 pv = *(const u32x2*)(op + 16 * dt); f32x4 v = sw[rb].o[dt] * sc2;
;                         v[0] += __uint_as_float(pv.x << 16); v[1] += __uint_as_float(pv.x & 0xffff0000u); v[2] += __uint_as_float(pv.y << 16); v[3] += __uint_as_float(pv.y & 0xffff0000u);
;                         *(unsigned*)(o8 + 16 * dt) = pk4_fp8(clamp8(v[0] * X8_SCALE), clamp8(v[1] * X8_SCALE), clamp8(v[2] * X8_SCALE), clamp8(v[3] * X8_SCALE)); } }
.LBB0_2176:
	ds_bpermute_b32 v1, v243, v62
	v_mov_b32_e32 v2, 0
	v_ashrrev_i32_e32 v109, 31, v108
	v_mov_b32_e32 v10, 0
	s_waitcnt lgkmcnt(0)
	v_cmp_lt_f32_e32 vcc, 0, v1
	s_and_saveexec_b64 s[0:1], vcc
	s_cbranch_execz .LBB0_2178
	v_readlane_b32 s2, v252, 59
	v_readlane_b32 s3, v252, 60
	s_movk_i32 s4, 0xc0
	s_nop 0
	v_lshl_add_u64 v[4:5], s[2:3], 0, v[108:109]
	v_mad_u64_u32 v[10:11], s[2:3], v4, s4, v[174:175]
	v_mad_i32_i24 v11, v5, s4, v11
	global_load_dword v4, v[10:11], off offset:8
	s_waitcnt vmcnt(0)
	v_rcp_f32_e32 v5, v1
	s_nop 0
	v_mul_f32_e32 v10, v4, v5
.LBB0_2178:
	s_or_b64 exec, exec, s[0:1]
	v_readlane_b32 s6, v252, 63
	v_lshlrev_b64 v[4:5], 10, v[108:109]
	v_readlane_b32 s7, v251, 0
	v_pk_mul_f32 v[16:17], v[60:61], v[10:11] op_sel_hi:[1,0]
	v_pk_mul_f32 v[18:19], v[58:59], v[10:11] op_sel_hi:[1,0]
	v_lshl_add_u64 v[4:5], v[4:5], 0, s[6:7]
	v_lshl_add_u64 v[12:13], v[4:5], 1, v[172:173]
	global_load_dwordx2 v[14:15], v[12:13], off
	global_load_dwordx2 v[66:67], v[12:13], off offset:32
	global_load_dwordx2 v[68:69], v[12:13], off offset:64
	global_load_dwordx2 v[70:71], v[12:13], off offset:96
	s_mov_b32 s5, 0xc3e00000
	v_lshl_add_u64 v[4:5], v[204:205], 0, v[4:5]
	v_ashrrev_i32_e32 v107, 31, v106
	s_waitcnt vmcnt(0)
	v_lshlrev_b32_e32 v1, 16, v14
	v_and_b32_e32 v11, 0xffff0000, v14
	v_add_f32_e32 v1, v18, v1
	v_add_f32_e32 v11, v19, v11
	v_lshlrev_b32_e32 v14, 16, v15
	v_mul_f32_e32 v1, 0x41000000, v1
	v_mul_f32_e32 v11, 0x41000000, v11
	v_add_f32_e32 v14, v16, v14
	v_med3_f32 v1, v1, s5, v249
	v_med3_f32 v11, v11, s5, v249
	v_mov_b32_e32 v16, v3
	v_and_b32_e32 v15, 0xffff0000, v15
	v_cvt_pk_fp8_f32 v16, v1, v11
	v_add_f32_e32 v15, v17, v15
	v_mul_f32_e32 v14, 0x41000000, v14
	v_mul_f32_e32 v15, 0x41000000, v15
	v_med3_f32 v14, v14, s5, v249
	v_med3_f32 v15, v15, s5, v249
	v_cvt_pk_fp8_f32 v16, v14, v15 op_sel:[0,0,1]
	v_pk_mul_f32 v[18:19], v[54:55], v[10:11] op_sel_hi:[1,0]
	global_store_dword v[4:5], v16, off
	v_pk_mul_f32 v[16:17], v[56:57], v[10:11] op_sel_hi:[1,0]
	v_lshlrev_b32_e32 v1, 16, v66
	v_and_b32_e32 v11, 0xffff0000, v66
	v_add_f32_e32 v1, v18, v1
	v_add_f32_e32 v11, v19, v11
	v_lshlrev_b32_e32 v14, 16, v67
	v_mul_f32_e32 v1, 0x41000000, v1
	v_mul_f32_e32 v11, 0x41000000, v11
	v_add_f32_e32 v14, v16, v14
	v_med3_f32 v1, v1, s5, v249
	v_med3_f32 v11, v11, s5, v249
	v_mov_b32_e32 v16, v3
	v_and_b32_e32 v15, 0xffff0000, v67
	v_cvt_pk_fp8_f32 v16, v1, v11
	v_add_f32_e32 v15, v17, v15
	v_mul_f32_e32 v14, 0x41000000, v14
	v_mul_f32_e32 v15, 0x41000000, v15
	v_med3_f32 v14, v14, s5, v249
	v_med3_f32 v15, v15, s5, v249
	v_cvt_pk_fp8_f32 v16, v14, v15 op_sel:[0,0,1]
	v_pk_mul_f32 v[18:19], v[46:47], v[10:11] op_sel_hi:[1,0]
	global_store_dword v[4:5], v16, off offset:16
	v_pk_mul_f32 v[16:17], v[48:49], v[10:11] op_sel_hi:[1,0]
	v_lshlrev_b32_e32 v1, 16, v68
	v_and_b32_e32 v11, 0xffff0000, v68
	v_add_f32_e32 v1, v18, v1
	v_add_f32_e32 v11, v19, v11
	v_lshlrev_b32_e32 v14, 16, v69
	v_mul_f32_e32 v1, 0x41000000, v1
	v_mul_f32_e32 v11, 0x41000000, v11
	v_add_f32_e32 v14, v16, v14
	v_med3_f32 v1, v1, s5, v249
	v_med3_f32 v11, v11, s5, v249
	v_mov_b32_e32 v16, v3
	v_and_b32_e32 v15, 0xffff0000, v69
	v_cvt_pk_fp8_f32 v16, v1, v11
	v_add_f32_e32 v15, v17, v15
	v_mul_f32_e32 v14, 0x41000000, v14
	v_mul_f32_e32 v15, 0x41000000, v15
	v_med3_f32 v14, v14, s5, v249
	v_med3_f32 v15, v15, s5, v249
	v_cvt_pk_fp8_f32 v16, v14, v15 op_sel:[0,0,1]
	v_pk_mul_f32 v[14:15], v[52:53], v[10:11] op_sel_hi:[1,0]
	v_pk_mul_f32 v[10:11], v[50:51], v[10:11] op_sel_hi:[1,0]
	global_store_dword v[4:5], v16, off offset:32
	v_lshlrev_b32_e32 v1, 16, v70
	v_add_f32_e32 v1, v10, v1
	v_and_b32_e32 v10, 0xffff0000, v70
	v_add_f32_e32 v10, v11, v10
	v_mul_f32_e32 v1, 0x41000000, v1
	v_mul_f32_e32 v10, 0x41000000, v10
	v_lshlrev_b32_e32 v11, 16, v71
	v_and_b32_e32 v12, 0xffff0000, v71
	v_med3_f32 v1, v1, s5, v249
	v_med3_f32 v10, v10, s5, v249
	v_mov_b32_e32 v13, v3
	v_cvt_pk_fp8_f32 v13, v1, v10
	v_add_f32_e32 v11, v14, v11
	v_add_f32_e32 v12, v15, v12
	v_mul_f32_e32 v11, 0x41000000, v11
	v_mul_f32_e32 v12, 0x41000000, v12
	ds_bpermute_b32 v1, v243, v38
	v_med3_f32 v11, v11, s5, v249
	v_med3_f32 v12, v12, s5, v249
	v_cvt_pk_fp8_f32 v13, v11, v12 op_sel:[0,0,1]
	s_waitcnt lgkmcnt(0)
	v_cmp_lt_f32_e32 vcc, 0, v1
	global_store_dword v[4:5], v13, off offset:48
	s_and_saveexec_b64 s[0:1], vcc
	v_readlane_b32 s58, v252, 7
	v_readlane_b32 s60, v252, 42
	v_readlane_b32 s62, v252, 44
	v_readlane_b32 s64, v252, 54
	v_readlane_b32 s59, v252, 8
	v_readlane_b32 s57, v252, 58
	v_readlane_b32 s61, v252, 43
	v_readlane_b32 s63, v252, 45
	v_readlane_b32 s65, v252, 55
	v_readlane_b32 s66, v252, 52
	v_readlane_b32 s67, v252, 53
	v_readlane_b32 s68, v252, 32
	v_readlane_b32 s69, v252, 33
	v_readlane_b32 s70, v251, 3
	s_cbranch_execz .LBB0_2180
	v_readlane_b32 s2, v252, 59
	v_readlane_b32 s3, v252, 60
	s_movk_i32 s4, 0xc0
	s_nop 0
	v_lshl_add_u64 v[4:5], s[2:3], 0, v[106:107]
	v_mad_u64_u32 v[10:11], s[2:3], v4, s4, v[174:175]
	v_mad_i32_i24 v11, v5, s4, v11
	global_load_dword v2, v[10:11], off offset:8
	s_waitcnt vmcnt(0)
	v_rcp_f32_e32 v4, v1
	s_nop 0
	v_mul_f32_e32 v2, v2, v4
